# cvt_wg: exact counted vmcnt for the 4-deep tile pipeline, drain only at the tail
# speedup vs baseline: 1.0114x; 1.0057x over previous
.LBB0_600:
	s_waitcnt vmcnt(24)
	v_pk_mul_f32 v[4:5], v[4:5], s[98:99]
	s_waitcnt vmcnt(24)
	v_pk_mul_f32 v[8:9], v[8:9], s[98:99]
	v_cvt_pk_fp8_f32 v1, v4, v8
	s_waitcnt vmcnt(24)
	v_pk_mul_f32 v[12:13], v[12:13], s[98:99]
	s_waitcnt vmcnt(24)
	v_pk_mul_f32 v[16:17], v[16:17], s[98:99]
	v_cvt_pk_fp8_f32 v1, v12, v16 op_sel:[0,0,1]
	v_cvt_pk_fp8_f32 v132, v5, v9
	v_pk_mul_f32 v[14:15], v[14:15], s[98:99]
	v_cvt_pk_fp8_f32 v132, v13, v17 op_sel:[0,0,1]
	v_pk_mul_f32 v[18:19], v[18:19], s[98:99]
	s_waitcnt vmcnt(24)
	v_pk_mul_f32 v[34:35], v[34:35], s[98:99]
	ds_write2_b32 v195, v1, v132 offset1:33
	v_pk_mul_f32 v[6:7], v[6:7], s[98:99]
	v_pk_mul_f32 v[10:11], v[10:11], s[98:99]
	v_cvt_pk_fp8_f32 v1, v6, v10
	s_add_i32 s28, s5, 4
	s_cmp_ge_u32 s28, s69
	v_cvt_pk_fp8_f32 v1, v14, v18 op_sel:[0,0,1]
	v_cvt_pk_fp8_f32 v132, v7, v11
	v_pk_mul_f32 v[28:29], v[28:29], s[98:99]
	s_cselect_b64 s[16:17], -1, 0
	v_cvt_pk_fp8_f32 v132, v15, v19 op_sel:[0,0,1]
	v_pk_mul_f32 v[32:33], v[32:33], s[98:99]
	s_and_b64 vcc, exec, s[16:17]
	ds_write2_b32 v195, v1, v132 offset0:66 offset1:99
	v_pk_mul_f32 v[20:21], v[20:21], s[98:99]
	v_pk_mul_f32 v[24:25], v[24:25], s[98:99]
	v_cvt_pk_fp8_f32 v1, v20, v24
	v_cvt_pk_fp8_f32 v1, v28, v32 op_sel:[0,0,1]
	v_cvt_pk_fp8_f32 v132, v21, v25
	v_pk_mul_f32 v[30:31], v[30:31], s[98:99]
	v_cvt_pk_fp8_f32 v132, v29, v33 op_sel:[0,0,1]
	v_add_u32_e32 v134, 0x2000, v195
	ds_write2_b32 v134, v1, v132 offset0:64 offset1:97
	v_pk_mul_f32 v[22:23], v[22:23], s[98:99]
	v_pk_mul_f32 v[26:27], v[26:27], s[98:99]
	v_cvt_pk_fp8_f32 v1, v22, v26
	v_cvt_pk_fp8_f32 v1, v30, v34 op_sel:[0,0,1]
	v_cvt_pk_fp8_f32 v132, v23, v27
	v_cvt_pk_fp8_f32 v132, v31, v35 op_sel:[0,0,1]
	ds_write2_b32 v134, v1, v132 offset0:130 offset1:163
	s_cbranch_vccz .Lcv1_ld_0
	s_waitcnt vmcnt(0)
	s_branch .LBB0_607
.Lcv1_ld_0:
	s_add_i32 s27, s8, s5
	s_add_i32 s26, s27, 4
	s_cmpk_gt_i32 s26, 0x3fff
	s_mov_b64 s[24:25], -1
	s_cbranch_scc0 .LBB0_603
	s_addk_i32 s27, 0xc004
	s_lshr_b32 s42, s27, 8
	s_add_i32 s14, s2, 32
	s_add_i32 s15, s4, 0x200
	v_readlane_b32 s52, v254, 31
	s_and_b32 s14, s14, 0x780
	s_and_b32 s24, s15, 0x600
	s_lshl_b64 s[22:23], s[42:43], 11
	s_lshl_b64 s[20:21], s[42:43], 24
	v_readlane_b32 s64, v254, 43
	v_readlane_b32 s65, v254, 44
	s_add_u32 s20, s64, s20
	s_addc_u32 s21, s65, s21
	s_lshl_b32 s25, s14, 13
	s_add_u32 s20, s20, s25
	s_addc_u32 s21, s21, 0
	s_lshl_b32 s25, s24, 2
	s_add_u32 s20, s20, s25
	v_readlane_b32 s53, v254, 32
	v_readlane_b32 s54, v254, 33
	v_readlane_b32 s55, v254, 34
	v_readlane_b32 s56, v254, 35
	v_readlane_b32 s57, v254, 36
	v_readlane_b32 s58, v254, 37
	v_readlane_b32 s59, v254, 38
	v_readlane_b32 s60, v254, 39
	v_readlane_b32 s61, v254, 40
	v_readlane_b32 s62, v254, 41
	v_readlane_b32 s63, v254, 42
	v_readlane_b32 s66, v254, 45
	v_readlane_b32 s67, v254, 46
	s_mov_b32 s15, s43
	s_addc_u32 s21, s21, 0
	s_or_b32 s22, s22, s24
	s_mov_b64 s[24:25], 0

.LBB0_610:
	s_waitcnt vmcnt(26)
	v_pk_mul_f32 v[36:37], v[36:37], s[98:99]
	s_waitcnt vmcnt(26)
	v_pk_mul_f32 v[40:41], v[40:41], s[98:99]
	v_cvt_pk_fp8_f32 v1, v36, v40
	s_waitcnt vmcnt(26)
	v_pk_mul_f32 v[44:45], v[44:45], s[98:99]
	s_waitcnt vmcnt(26)
	v_pk_mul_f32 v[52:53], v[52:53], s[98:99]
	v_cvt_pk_fp8_f32 v1, v44, v52 op_sel:[0,0,1]
	v_cvt_pk_fp8_f32 v135, v37, v41
	v_add_u32_e32 v136, 0x4000, v195
	v_cvt_pk_fp8_f32 v135, v45, v53 op_sel:[0,0,1]
	v_pk_mul_f32 v[46:47], v[46:47], s[98:99]
	v_pk_mul_f32 v[54:55], v[54:55], s[98:99]
	ds_write2_b32 v136, v1, v135 offset0:128 offset1:161
	v_pk_mul_f32 v[38:39], v[38:39], s[98:99]
	v_pk_mul_f32 v[42:43], v[42:43], s[98:99]
	v_cvt_pk_fp8_f32 v1, v38, v42
	s_add_i32 s18, s5, 5
	s_cmp_ge_u32 s18, s69
	v_cvt_pk_fp8_f32 v1, v46, v54 op_sel:[0,0,1]
	v_cvt_pk_fp8_f32 v135, v39, v43
	s_waitcnt vmcnt(26)
	v_pk_mul_f32 v[64:65], v[64:65], s[98:99]
	s_mov_b64 s[18:19], s[10:11]
	v_cvt_pk_fp8_f32 v135, v47, v55 op_sel:[0,0,1]
	ds_write2_b32 v136, v1, v135 offset0:194 offset1:227
	v_pk_mul_f32 v[48:49], v[48:49], s[98:99]
	v_pk_mul_f32 v[56:57], v[56:57], s[98:99]
	v_cvt_pk_fp8_f32 v1, v48, v56
	v_pk_mul_f32 v[60:61], v[60:61], s[98:99]
	v_cvt_pk_fp8_f32 v1, v60, v64 op_sel:[0,0,1]
	v_cvt_pk_fp8_f32 v135, v49, v57
	v_add_u32_e32 v136, 0x6000, v195
	v_cvt_pk_fp8_f32 v135, v61, v65 op_sel:[0,0,1]
	v_pk_mul_f32 v[66:67], v[66:67], s[98:99]
	ds_write2_b32 v136, v1, v135 offset0:192 offset1:225
	v_pk_mul_f32 v[50:51], v[50:51], s[98:99]
	v_pk_mul_f32 v[58:59], v[58:59], s[98:99]
	v_cvt_pk_fp8_f32 v1, v50, v58
	v_pk_mul_f32 v[62:63], v[62:63], s[98:99]
	v_cvt_pk_fp8_f32 v1, v62, v66 op_sel:[0,0,1]
	v_cvt_pk_fp8_f32 v135, v51, v59
	v_add_u32_e32 v136, 0x6400, v195
	v_cvt_pk_fp8_f32 v135, v63, v67 op_sel:[0,0,1]
	ds_write2_b32 v136, v1, v135 offset0:2 offset1:35
	s_cbranch_scc0 .Lcv1_ld_1
	s_waitcnt vmcnt(0)
	s_branch .LBB0_617
.Lcv1_ld_1:
	s_add_i32 s27, s8, s5
	s_add_i32 s26, s27, 5
	s_cmpk_gt_i32 s26, 0x3fff
	s_mov_b64 s[24:25], -1
	s_cbranch_scc0 .LBB0_613
	s_addk_i32 s27, 0xc005
	s_lshr_b32 s42, s27, 8
	s_add_i32 s18, s2, 40
	s_add_i32 s19, s4, 0x280
	v_readlane_b32 s52, v254, 31
	s_and_b32 s18, s18, 0x780
	s_and_b32 s24, s19, 0x680
	s_lshl_b64 s[22:23], s[42:43], 11
	s_lshl_b64 s[20:21], s[42:43], 24
	v_readlane_b32 s64, v254, 43
	v_readlane_b32 s65, v254, 44
	s_add_u32 s20, s64, s20
	s_addc_u32 s21, s65, s21
	s_lshl_b32 s25, s18, 13
	s_add_u32 s20, s20, s25
	s_addc_u32 s21, s21, 0
	s_lshl_b32 s25, s24, 2
	s_add_u32 s20, s20, s25
	v_readlane_b32 s53, v254, 32
	v_readlane_b32 s54, v254, 33
	v_readlane_b32 s55, v254, 34
	v_readlane_b32 s56, v254, 35
	v_readlane_b32 s57, v254, 36
	v_readlane_b32 s58, v254, 37
	v_readlane_b32 s59, v254, 38
	v_readlane_b32 s60, v254, 39
	v_readlane_b32 s61, v254, 40
	v_readlane_b32 s62, v254, 41
	v_readlane_b32 s63, v254, 42
	v_readlane_b32 s66, v254, 45
	v_readlane_b32 s67, v254, 46
	s_mov_b32 s19, s43
	s_addc_u32 s21, s21, 0
	s_or_b32 s22, s22, s24
	s_mov_b64 s[24:25], 0

.LBB0_618:
	s_waitcnt vmcnt(28)
	v_pk_mul_f32 v[68:69], v[68:69], s[98:99]
	s_waitcnt vmcnt(28)
	v_pk_mul_f32 v[72:73], v[72:73], s[98:99]
	v_cvt_pk_fp8_f32 v1, v68, v72
	s_waitcnt vmcnt(28)
	v_pk_mul_f32 v[76:77], v[76:77], s[98:99]
	s_waitcnt vmcnt(28)
	v_pk_mul_f32 v[84:85], v[84:85], s[98:99]
	v_cvt_pk_fp8_f32 v1, v76, v84 op_sel:[0,0,1]
	v_cvt_pk_fp8_f32 v135, v69, v73
	v_pk_mul_f32 v[78:79], v[78:79], s[98:99]
	v_cvt_pk_fp8_f32 v135, v77, v85 op_sel:[0,0,1]
	v_pk_mul_f32 v[86:87], v[86:87], s[98:99]
	s_add_i32 s18, s5, 6
	ds_write2_b32 v195, v1, v135 offset1:33
	v_pk_mul_f32 v[70:71], v[70:71], s[98:99]
	v_pk_mul_f32 v[74:75], v[74:75], s[98:99]
	v_cvt_pk_fp8_f32 v1, v70, v74
	s_cmp_ge_u32 s18, s69
	s_mov_b64 s[18:19], s[0:1]
	v_cvt_pk_fp8_f32 v1, v78, v86 op_sel:[0,0,1]
	v_cvt_pk_fp8_f32 v135, v71, v75
	s_waitcnt vmcnt(28)
	v_pk_mul_f32 v[92:93], v[92:93], s[98:99]
	v_cvt_pk_fp8_f32 v135, v79, v87 op_sel:[0,0,1]
	s_waitcnt vmcnt(28)
	v_pk_mul_f32 v[96:97], v[96:97], s[98:99]
	ds_write2_b32 v195, v1, v135 offset0:66 offset1:99
	v_pk_mul_f32 v[80:81], v[80:81], s[98:99]
	v_pk_mul_f32 v[88:89], v[88:89], s[98:99]
	v_cvt_pk_fp8_f32 v1, v80, v88
	v_cvt_pk_fp8_f32 v1, v92, v96 op_sel:[0,0,1]
	v_cvt_pk_fp8_f32 v135, v81, v89
	v_pk_mul_f32 v[94:95], v[94:95], s[98:99]
	v_cvt_pk_fp8_f32 v135, v93, v97 op_sel:[0,0,1]
	v_pk_mul_f32 v[98:99], v[98:99], s[98:99]
	ds_write2_b32 v134, v1, v135 offset0:64 offset1:97
	v_pk_mul_f32 v[82:83], v[82:83], s[98:99]
	v_pk_mul_f32 v[90:91], v[90:91], s[98:99]
	v_cvt_pk_fp8_f32 v1, v82, v90
	v_cvt_pk_fp8_f32 v1, v94, v98 op_sel:[0,0,1]
	v_cvt_pk_fp8_f32 v135, v83, v91
	v_cvt_pk_fp8_f32 v135, v95, v99 op_sel:[0,0,1]
	ds_write2_b32 v134, v1, v135 offset0:130 offset1:163
	s_cbranch_scc0 .Lcv1_ld_2
	s_waitcnt vmcnt(0)
	s_branch .LBB0_625
.Lcv1_ld_2:
	s_add_i32 s27, s8, s5
	s_add_i32 s26, s27, 6
	s_cmpk_gt_i32 s26, 0x3fff
	s_mov_b64 s[24:25], -1
	s_cbranch_scc0 .LBB0_621
	s_addk_i32 s27, 0xc006
	s_lshr_b32 s42, s27, 8
	s_add_i32 s18, s2, 48
	s_add_i32 s19, s4, 0x300
	v_readlane_b32 s52, v254, 31
	s_and_b32 s18, s18, 0x780
	s_and_b32 s24, s19, 0x700
	s_lshl_b64 s[22:23], s[42:43], 11
	s_lshl_b64 s[20:21], s[42:43], 24
	v_readlane_b32 s64, v254, 43
	v_readlane_b32 s65, v254, 44
	s_add_u32 s20, s64, s20
	s_addc_u32 s21, s65, s21
	s_lshl_b32 s25, s18, 13
	s_add_u32 s20, s20, s25
	s_addc_u32 s21, s21, 0
	s_lshl_b32 s25, s24, 2
	s_add_u32 s20, s20, s25
	v_readlane_b32 s53, v254, 32
	v_readlane_b32 s54, v254, 33
	v_readlane_b32 s55, v254, 34
	v_readlane_b32 s56, v254, 35
	v_readlane_b32 s57, v254, 36
	v_readlane_b32 s58, v254, 37
	v_readlane_b32 s59, v254, 38
	v_readlane_b32 s60, v254, 39
	v_readlane_b32 s61, v254, 40
	v_readlane_b32 s62, v254, 41
	v_readlane_b32 s63, v254, 42
	v_readlane_b32 s66, v254, 45
	v_readlane_b32 s67, v254, 46
	s_mov_b32 s19, s43
	s_addc_u32 s21, s21, 0
	s_or_b32 s22, s22, s24
	s_mov_b64 s[24:25], 0

.LBB0_626:
	s_waitcnt vmcnt(30)
	v_pk_mul_f32 v[108:109], v[108:109], s[98:99]
	v_pk_mul_f32 v[100:101], v[100:101], s[98:99]
	v_cvt_pk_fp8_f32 v1, v108, v100
	v_pk_mul_f32 v[104:105], v[104:105], s[98:99]
	s_waitcnt vmcnt(30)
	v_pk_mul_f32 v[116:117], v[116:117], s[98:99]
	v_cvt_pk_fp8_f32 v1, v104, v116 op_sel:[0,0,1]
	v_cvt_pk_fp8_f32 v134, v109, v101
	v_add_u32_e32 v135, 0x4000, v195
	v_cvt_pk_fp8_f32 v134, v105, v117 op_sel:[0,0,1]
	v_pk_mul_f32 v[106:107], v[106:107], s[98:99]
	v_pk_mul_f32 v[118:119], v[118:119], s[98:99]
	ds_write2_b32 v135, v1, v134 offset0:128 offset1:161
	v_pk_mul_f32 v[110:111], v[110:111], s[98:99]
	v_pk_mul_f32 v[102:103], v[102:103], s[98:99]
	v_cvt_pk_fp8_f32 v1, v110, v102
	s_add_i32 s18, s5, 7
	s_cmp_ge_u32 s18, s69
	v_cvt_pk_fp8_f32 v1, v106, v118 op_sel:[0,0,1]
	v_cvt_pk_fp8_f32 v134, v111, v103
	s_waitcnt vmcnt(30)
	v_pk_mul_f32 v[128:129], v[128:129], s[98:99]
	s_mov_b64 s[18:19], s[12:13]
	v_cvt_pk_fp8_f32 v134, v107, v119 op_sel:[0,0,1]
	ds_write2_b32 v135, v1, v134 offset0:194 offset1:227
	v_pk_mul_f32 v[112:113], v[112:113], s[98:99]
	v_pk_mul_f32 v[120:121], v[120:121], s[98:99]
	v_cvt_pk_fp8_f32 v1, v112, v120
	v_pk_mul_f32 v[124:125], v[124:125], s[98:99]
	v_cvt_pk_fp8_f32 v1, v124, v128 op_sel:[0,0,1]
	v_cvt_pk_fp8_f32 v134, v113, v121
	v_add_u32_e32 v135, 0x6000, v195
	v_cvt_pk_fp8_f32 v134, v125, v129 op_sel:[0,0,1]
	v_pk_mul_f32 v[130:131], v[130:131], s[98:99]
	ds_write2_b32 v135, v1, v134 offset0:192 offset1:225
	v_pk_mul_f32 v[114:115], v[114:115], s[98:99]
	v_pk_mul_f32 v[122:123], v[122:123], s[98:99]
	v_cvt_pk_fp8_f32 v1, v114, v122
	v_pk_mul_f32 v[126:127], v[126:127], s[98:99]
	v_cvt_pk_fp8_f32 v1, v126, v130 op_sel:[0,0,1]
	v_cvt_pk_fp8_f32 v134, v115, v123
	v_add_u32_e32 v135, 0x6400, v195
	v_cvt_pk_fp8_f32 v134, v127, v131 op_sel:[0,0,1]
	ds_write2_b32 v135, v1, v134 offset0:2 offset1:35
	s_cbranch_scc0 .Lcv1_ld_3
	s_waitcnt vmcnt(0)
	s_branch .LBB0_598
.Lcv1_ld_3:
	s_add_i32 s26, s8, s5
	s_add_i32 s5, s26, 7
	s_cmpk_gt_i32 s5, 0x3fff
	s_mov_b64 s[24:25], -1
	s_cbranch_scc0 .LBB0_629
	s_addk_i32 s26, 0xc007
	s_lshr_b32 s42, s26, 8
	s_add_i32 s18, s2, 56
	s_add_i32 s19, s4, 0x380
	v_readlane_b32 s52, v254, 31
	s_and_b32 s18, s18, 0x780
	s_and_b32 s24, s19, 0x780
	s_lshl_b64 s[22:23], s[42:43], 11
	s_lshl_b64 s[20:21], s[42:43], 24
	v_readlane_b32 s64, v254, 43
	v_readlane_b32 s65, v254, 44
	s_add_u32 s20, s64, s20
	s_addc_u32 s21, s65, s21
	s_lshl_b32 s25, s18, 13
	s_add_u32 s20, s20, s25
	s_addc_u32 s21, s21, 0
	s_lshl_b32 s25, s24, 2
	s_add_u32 s20, s20, s25
	v_readlane_b32 s53, v254, 32
	v_readlane_b32 s54, v254, 33
	v_readlane_b32 s55, v254, 34
	v_readlane_b32 s56, v254, 35
	v_readlane_b32 s57, v254, 36
	v_readlane_b32 s58, v254, 37
	v_readlane_b32 s59, v254, 38
	v_readlane_b32 s60, v254, 39
	v_readlane_b32 s61, v254, 40
	v_readlane_b32 s62, v254, 41
	v_readlane_b32 s63, v254, 42
	v_readlane_b32 s66, v254, 45
	v_readlane_b32 s67, v254, 46
	s_mov_b32 s19, s43
	s_addc_u32 s21, s21, 0
	s_or_b32 s22, s22, s24
	s_mov_b64 s[24:25], 0

.LBB0_754:
	s_waitcnt vmcnt(24)
	v_pk_mul_f32 v[12:13], v[12:13], s[98:99]
	v_pk_mul_f32 v[4:5], v[4:5], s[98:99]
	v_cvt_pk_fp8_f32 v1, v12, v4
	v_pk_mul_f32 v[8:9], v[8:9], s[98:99]
	s_waitcnt vmcnt(24)
	v_pk_mul_f32 v[20:21], v[20:21], s[98:99]
	v_cvt_pk_fp8_f32 v1, v8, v20 op_sel:[0,0,1]
	v_cvt_pk_fp8_f32 v132, v13, v5
	v_pk_mul_f32 v[10:11], v[10:11], s[98:99]
	v_cvt_pk_fp8_f32 v132, v9, v21 op_sel:[0,0,1]
	v_pk_mul_f32 v[22:23], v[22:23], s[98:99]
	s_waitcnt vmcnt(24)
	v_pk_mul_f32 v[34:35], v[34:35], s[98:99]
	ds_write2_b32 v195, v1, v132 offset1:33
	v_pk_mul_f32 v[14:15], v[14:15], s[98:99]
	v_pk_mul_f32 v[6:7], v[6:7], s[98:99]
	v_cvt_pk_fp8_f32 v1, v14, v6
	s_add_i32 s9, s5, 4
	s_cmp_ge_u32 s9, s71
	v_cvt_pk_fp8_f32 v1, v10, v22 op_sel:[0,0,1]
	v_cvt_pk_fp8_f32 v132, v15, v7
	v_pk_mul_f32 v[28:29], v[28:29], s[98:99]
	s_cselect_b64 s[16:17], -1, 0
	v_cvt_pk_fp8_f32 v132, v11, v23 op_sel:[0,0,1]
	v_pk_mul_f32 v[32:33], v[32:33], s[98:99]
	s_and_b64 vcc, exec, s[16:17]
	ds_write2_b32 v195, v1, v132 offset0:66 offset1:99
	v_pk_mul_f32 v[16:17], v[16:17], s[98:99]
	v_pk_mul_f32 v[24:25], v[24:25], s[98:99]
	v_cvt_pk_fp8_f32 v1, v16, v24
	v_cvt_pk_fp8_f32 v1, v28, v32 op_sel:[0,0,1]
	v_cvt_pk_fp8_f32 v132, v17, v25
	v_pk_mul_f32 v[30:31], v[30:31], s[98:99]
	v_cvt_pk_fp8_f32 v132, v29, v33 op_sel:[0,0,1]
	v_add_u32_e32 v134, 0x2000, v195
	ds_write2_b32 v134, v1, v132 offset0:64 offset1:97
	v_pk_mul_f32 v[18:19], v[18:19], s[98:99]
	v_pk_mul_f32 v[26:27], v[26:27], s[98:99]
	v_cvt_pk_fp8_f32 v1, v18, v26
	v_cvt_pk_fp8_f32 v1, v30, v34 op_sel:[0,0,1]
	v_cvt_pk_fp8_f32 v132, v19, v27
	v_cvt_pk_fp8_f32 v132, v31, v35 op_sel:[0,0,1]
	ds_write2_b32 v134, v1, v132 offset0:130 offset1:163
	s_cbranch_vccz .Lcv2_ld_0
	s_waitcnt vmcnt(0)
	s_branch .LBB0_761
.Lcv2_ld_0:
	s_add_i32 s27, s8, s5
	s_add_i32 s26, s27, 4
	s_cmpk_gt_i32 s26, 0x3fff
	s_mov_b64 s[24:25], -1
	s_cbranch_scc0 .LBB0_757
	s_addk_i32 s27, 0xc004
	s_lshr_b32 s42, s27, 8
	s_add_i32 s14, s2, 32
	s_add_i32 s15, s4, 0x200
	v_readlane_b32 s48, v254, 31
	s_and_b32 s14, s14, 0x780
	s_and_b32 s24, s15, 0x700
	s_lshl_b64 s[22:23], s[42:43], 11
	s_lshl_b64 s[20:21], s[42:43], 24
	v_readlane_b32 s60, v254, 43
	v_readlane_b32 s61, v254, 44
	s_add_u32 s20, s60, s20
	s_addc_u32 s21, s61, s21
	s_lshl_b32 s25, s14, 13
	s_add_u32 s20, s20, s25
	s_addc_u32 s21, s21, 0
	s_lshl_b32 s25, s24, 2
	s_add_u32 s20, s20, s25
	v_readlane_b32 s49, v254, 32
	v_readlane_b32 s50, v254, 33
	v_readlane_b32 s51, v254, 34
	v_readlane_b32 s52, v254, 35
	v_readlane_b32 s53, v254, 36
	v_readlane_b32 s54, v254, 37
	v_readlane_b32 s55, v254, 38
	v_readlane_b32 s56, v254, 39
	v_readlane_b32 s57, v254, 40
	v_readlane_b32 s58, v254, 41
	v_readlane_b32 s59, v254, 42
	v_readlane_b32 s62, v254, 45
	v_readlane_b32 s63, v254, 46
	s_mov_b32 s15, s43
	s_addc_u32 s21, s21, 0
	s_or_b32 s22, s22, s24
	s_mov_b64 s[24:25], 0

.LBB0_764:
	s_waitcnt vmcnt(26)
	v_pk_mul_f32 v[44:45], v[44:45], s[98:99]
	v_pk_mul_f32 v[36:37], v[36:37], s[98:99]
	v_cvt_pk_fp8_f32 v1, v44, v36
	v_pk_mul_f32 v[40:41], v[40:41], s[98:99]
	s_waitcnt vmcnt(26)
	v_pk_mul_f32 v[52:53], v[52:53], s[98:99]
	v_cvt_pk_fp8_f32 v1, v40, v52 op_sel:[0,0,1]
	v_cvt_pk_fp8_f32 v135, v45, v37
	v_add_u32_e32 v136, 0x4000, v195
	v_cvt_pk_fp8_f32 v135, v41, v53 op_sel:[0,0,1]
	v_pk_mul_f32 v[42:43], v[42:43], s[98:99]
	v_pk_mul_f32 v[54:55], v[54:55], s[98:99]
	ds_write2_b32 v136, v1, v135 offset0:128 offset1:161
	v_pk_mul_f32 v[46:47], v[46:47], s[98:99]
	v_pk_mul_f32 v[38:39], v[38:39], s[98:99]
	v_cvt_pk_fp8_f32 v1, v46, v38
	s_add_i32 s18, s5, 5
	s_cmp_ge_u32 s18, s71
	v_cvt_pk_fp8_f32 v1, v42, v54 op_sel:[0,0,1]
	v_cvt_pk_fp8_f32 v135, v47, v39
	s_waitcnt vmcnt(26)
	v_pk_mul_f32 v[64:65], v[64:65], s[98:99]
	s_mov_b64 s[18:19], s[10:11]
	v_cvt_pk_fp8_f32 v135, v43, v55 op_sel:[0,0,1]
	ds_write2_b32 v136, v1, v135 offset0:194 offset1:227
	v_pk_mul_f32 v[48:49], v[48:49], s[98:99]
	v_pk_mul_f32 v[56:57], v[56:57], s[98:99]
	v_cvt_pk_fp8_f32 v1, v48, v56
	v_pk_mul_f32 v[60:61], v[60:61], s[98:99]
	v_cvt_pk_fp8_f32 v1, v60, v64 op_sel:[0,0,1]
	v_cvt_pk_fp8_f32 v135, v49, v57
	v_add_u32_e32 v136, 0x6000, v195
	v_cvt_pk_fp8_f32 v135, v61, v65 op_sel:[0,0,1]
	v_pk_mul_f32 v[66:67], v[66:67], s[98:99]
	ds_write2_b32 v136, v1, v135 offset0:192 offset1:225
	v_pk_mul_f32 v[50:51], v[50:51], s[98:99]
	v_pk_mul_f32 v[58:59], v[58:59], s[98:99]
	v_cvt_pk_fp8_f32 v1, v50, v58
	v_pk_mul_f32 v[62:63], v[62:63], s[98:99]
	v_cvt_pk_fp8_f32 v1, v62, v66 op_sel:[0,0,1]
	v_cvt_pk_fp8_f32 v135, v51, v59
	v_add_u32_e32 v136, 0x6400, v195
	v_cvt_pk_fp8_f32 v135, v63, v67 op_sel:[0,0,1]
	ds_write2_b32 v136, v1, v135 offset0:2 offset1:35
	s_cbranch_scc0 .Lcv2_ld_1
	s_waitcnt vmcnt(0)
	s_branch .LBB0_771
.Lcv2_ld_1:
	s_add_i32 s27, s8, s5
	s_add_i32 s26, s27, 5
	s_cmpk_gt_i32 s26, 0x3fff
	s_mov_b64 s[24:25], -1
	s_cbranch_scc0 .LBB0_767
	s_addk_i32 s27, 0xc005
	s_lshr_b32 s42, s27, 8
	s_add_i32 s18, s2, 40
	s_add_i32 s19, s4, 0x280
	v_readlane_b32 s48, v254, 31
	s_and_b32 s18, s18, 0x780
	s_and_b32 s24, s19, 0x780
	s_lshl_b64 s[22:23], s[42:43], 11
	s_lshl_b64 s[20:21], s[42:43], 24
	v_readlane_b32 s60, v254, 43
	v_readlane_b32 s61, v254, 44
	s_add_u32 s20, s60, s20
	s_addc_u32 s21, s61, s21
	s_lshl_b32 s25, s18, 13
	s_add_u32 s20, s20, s25
	s_addc_u32 s21, s21, 0
	s_lshl_b32 s25, s24, 2
	s_add_u32 s20, s20, s25
	v_readlane_b32 s49, v254, 32
	v_readlane_b32 s50, v254, 33
	v_readlane_b32 s51, v254, 34
	v_readlane_b32 s52, v254, 35
	v_readlane_b32 s53, v254, 36
	v_readlane_b32 s54, v254, 37
	v_readlane_b32 s55, v254, 38
	v_readlane_b32 s56, v254, 39
	v_readlane_b32 s57, v254, 40
	v_readlane_b32 s58, v254, 41
	v_readlane_b32 s59, v254, 42
	v_readlane_b32 s62, v254, 45
	v_readlane_b32 s63, v254, 46
	s_mov_b32 s19, s43
	s_addc_u32 s21, s21, 0
	s_or_b32 s22, s22, s24
	s_mov_b64 s[24:25], 0

.LBB0_772:
	s_waitcnt vmcnt(28)
	v_pk_mul_f32 v[76:77], v[76:77], s[98:99]
	v_pk_mul_f32 v[68:69], v[68:69], s[98:99]
	v_cvt_pk_fp8_f32 v1, v76, v68
	v_pk_mul_f32 v[72:73], v[72:73], s[98:99]
	s_waitcnt vmcnt(28)
	v_pk_mul_f32 v[84:85], v[84:85], s[98:99]
	v_cvt_pk_fp8_f32 v1, v72, v84 op_sel:[0,0,1]
	v_cvt_pk_fp8_f32 v135, v77, v69
	v_pk_mul_f32 v[74:75], v[74:75], s[98:99]
	v_cvt_pk_fp8_f32 v135, v73, v85 op_sel:[0,0,1]
	v_pk_mul_f32 v[86:87], v[86:87], s[98:99]
	s_add_i32 s18, s5, 6
	ds_write2_b32 v195, v1, v135 offset1:33
	v_pk_mul_f32 v[78:79], v[78:79], s[98:99]
	v_pk_mul_f32 v[70:71], v[70:71], s[98:99]
	v_cvt_pk_fp8_f32 v1, v78, v70
	s_cmp_ge_u32 s18, s71
	s_mov_b64 s[18:19], s[0:1]
	v_cvt_pk_fp8_f32 v1, v74, v86 op_sel:[0,0,1]
	v_cvt_pk_fp8_f32 v135, v79, v71
	s_waitcnt vmcnt(28)
	v_pk_mul_f32 v[92:93], v[92:93], s[98:99]
	v_cvt_pk_fp8_f32 v135, v75, v87 op_sel:[0,0,1]
	s_waitcnt vmcnt(28)
	v_pk_mul_f32 v[96:97], v[96:97], s[98:99]
	ds_write2_b32 v195, v1, v135 offset0:66 offset1:99
	v_pk_mul_f32 v[80:81], v[80:81], s[98:99]
	v_pk_mul_f32 v[88:89], v[88:89], s[98:99]
	v_cvt_pk_fp8_f32 v1, v80, v88
	v_cvt_pk_fp8_f32 v1, v92, v96 op_sel:[0,0,1]
	v_cvt_pk_fp8_f32 v135, v81, v89
	v_pk_mul_f32 v[94:95], v[94:95], s[98:99]
	v_cvt_pk_fp8_f32 v135, v93, v97 op_sel:[0,0,1]
	v_pk_mul_f32 v[98:99], v[98:99], s[98:99]
	ds_write2_b32 v134, v1, v135 offset0:64 offset1:97
	v_pk_mul_f32 v[82:83], v[82:83], s[98:99]
	v_pk_mul_f32 v[90:91], v[90:91], s[98:99]
	v_cvt_pk_fp8_f32 v1, v82, v90
	v_cvt_pk_fp8_f32 v1, v94, v98 op_sel:[0,0,1]
	v_cvt_pk_fp8_f32 v135, v83, v91
	v_cvt_pk_fp8_f32 v135, v95, v99 op_sel:[0,0,1]
	ds_write2_b32 v134, v1, v135 offset0:130 offset1:163
	s_cbranch_scc0 .Lcv2_ld_2
	s_waitcnt vmcnt(0)
	s_branch .LBB0_779
.Lcv2_ld_2:
	s_add_i32 s27, s8, s5
	s_add_i32 s26, s27, 6
	s_cmpk_gt_i32 s26, 0x3fff
	s_mov_b64 s[24:25], -1
	s_cbranch_scc0 .LBB0_775
	s_addk_i32 s27, 0xc006
	s_lshr_b32 s42, s27, 8
	s_add_i32 s18, s2, 48
	s_add_i32 s19, s4, 0x300
	v_readlane_b32 s48, v254, 31
	s_and_b32 s18, s18, 0x780
	s_and_b32 s24, s19, 0x700
	s_lshl_b64 s[22:23], s[42:43], 11
	s_lshl_b64 s[20:21], s[42:43], 24
	v_readlane_b32 s60, v254, 43
	v_readlane_b32 s61, v254, 44
	s_add_u32 s20, s60, s20
	s_addc_u32 s21, s61, s21
	s_lshl_b32 s25, s18, 13
	s_add_u32 s20, s20, s25
	s_addc_u32 s21, s21, 0
	s_lshl_b32 s25, s24, 2
	s_add_u32 s20, s20, s25
	v_readlane_b32 s49, v254, 32
	v_readlane_b32 s50, v254, 33
	v_readlane_b32 s51, v254, 34
	v_readlane_b32 s52, v254, 35
	v_readlane_b32 s53, v254, 36
	v_readlane_b32 s54, v254, 37
	v_readlane_b32 s55, v254, 38
	v_readlane_b32 s56, v254, 39
	v_readlane_b32 s57, v254, 40
	v_readlane_b32 s58, v254, 41
	v_readlane_b32 s59, v254, 42
	v_readlane_b32 s62, v254, 45
	v_readlane_b32 s63, v254, 46
	s_mov_b32 s19, s43
	s_addc_u32 s21, s21, 0
	s_or_b32 s22, s22, s24
	s_mov_b64 s[24:25], 0

.LBB0_780:
	s_waitcnt vmcnt(30)
	v_pk_mul_f32 v[108:109], v[108:109], s[98:99]
	v_pk_mul_f32 v[100:101], v[100:101], s[98:99]
	v_cvt_pk_fp8_f32 v1, v108, v100
	v_pk_mul_f32 v[104:105], v[104:105], s[98:99]
	s_waitcnt vmcnt(30)
	v_pk_mul_f32 v[116:117], v[116:117], s[98:99]
	v_cvt_pk_fp8_f32 v1, v104, v116 op_sel:[0,0,1]
	v_cvt_pk_fp8_f32 v134, v109, v101
	v_add_u32_e32 v135, 0x4000, v195
	v_cvt_pk_fp8_f32 v134, v105, v117 op_sel:[0,0,1]
	v_pk_mul_f32 v[106:107], v[106:107], s[98:99]
	v_pk_mul_f32 v[118:119], v[118:119], s[98:99]
	ds_write2_b32 v135, v1, v134 offset0:128 offset1:161
	v_pk_mul_f32 v[110:111], v[110:111], s[98:99]
	v_pk_mul_f32 v[102:103], v[102:103], s[98:99]
	v_cvt_pk_fp8_f32 v1, v110, v102
	s_add_i32 s18, s5, 7
	s_cmp_ge_u32 s18, s71
	v_cvt_pk_fp8_f32 v1, v106, v118 op_sel:[0,0,1]
	v_cvt_pk_fp8_f32 v134, v111, v103
	s_waitcnt vmcnt(30)
	v_pk_mul_f32 v[128:129], v[128:129], s[98:99]
	s_mov_b64 s[18:19], s[12:13]
	v_cvt_pk_fp8_f32 v134, v107, v119 op_sel:[0,0,1]
	ds_write2_b32 v135, v1, v134 offset0:194 offset1:227
	v_pk_mul_f32 v[112:113], v[112:113], s[98:99]
	v_pk_mul_f32 v[120:121], v[120:121], s[98:99]
	v_cvt_pk_fp8_f32 v1, v112, v120
	v_pk_mul_f32 v[124:125], v[124:125], s[98:99]
	v_cvt_pk_fp8_f32 v1, v124, v128 op_sel:[0,0,1]
	v_cvt_pk_fp8_f32 v134, v113, v121
	v_add_u32_e32 v135, 0x6000, v195
	v_cvt_pk_fp8_f32 v134, v125, v129 op_sel:[0,0,1]
	v_pk_mul_f32 v[130:131], v[130:131], s[98:99]
	ds_write2_b32 v135, v1, v134 offset0:192 offset1:225
	v_pk_mul_f32 v[114:115], v[114:115], s[98:99]
	v_pk_mul_f32 v[122:123], v[122:123], s[98:99]
	v_cvt_pk_fp8_f32 v1, v114, v122
	v_pk_mul_f32 v[126:127], v[126:127], s[98:99]
	v_cvt_pk_fp8_f32 v1, v126, v130 op_sel:[0,0,1]
	v_cvt_pk_fp8_f32 v134, v115, v123
	v_add_u32_e32 v135, 0x6400, v195
	v_cvt_pk_fp8_f32 v134, v127, v131 op_sel:[0,0,1]
	ds_write2_b32 v135, v1, v134 offset0:2 offset1:35
	s_cbranch_scc0 .Lcv2_ld_3
	s_waitcnt vmcnt(0)
	s_branch .LBB0_752
.Lcv2_ld_3:
	s_add_i32 s26, s8, s5
	s_add_i32 s5, s26, 7
	s_cmpk_gt_i32 s5, 0x3fff
	s_mov_b64 s[24:25], -1
	s_cbranch_scc0 .LBB0_783
	s_addk_i32 s26, 0xc007
	s_lshr_b32 s42, s26, 8
	s_add_i32 s18, s2, 56
	s_add_i32 s19, s4, 0x380
	v_readlane_b32 s48, v254, 31
	s_and_b32 s18, s18, 0x780
	s_and_b32 s24, s19, 0x780
	s_lshl_b64 s[22:23], s[42:43], 11
	s_lshl_b64 s[20:21], s[42:43], 24
	v_readlane_b32 s60, v254, 43
	v_readlane_b32 s61, v254, 44
	s_add_u32 s20, s60, s20
	s_addc_u32 s21, s61, s21
	s_lshl_b32 s25, s18, 13
	s_add_u32 s20, s20, s25
	s_addc_u32 s21, s21, 0
	s_lshl_b32 s25, s24, 2
	s_add_u32 s20, s20, s25
	v_readlane_b32 s49, v254, 32
	v_readlane_b32 s50, v254, 33
	v_readlane_b32 s51, v254, 34
	v_readlane_b32 s52, v254, 35
	v_readlane_b32 s53, v254, 36
	v_readlane_b32 s54, v254, 37
	v_readlane_b32 s55, v254, 38
	v_readlane_b32 s56, v254, 39
	v_readlane_b32 s57, v254, 40
	v_readlane_b32 s58, v254, 41
	v_readlane_b32 s59, v254, 42
	v_readlane_b32 s62, v254, 45
	v_readlane_b32 s63, v254, 46
	s_mov_b32 s19, s43
	s_addc_u32 s21, s21, 0
	s_or_b32 s22, s22, s24
	s_mov_b64 s[24:25], 0
